# P7 EpiResid epilogue: 32 serialized load-wait-store round trips replaced by a 3-row-deep load pipeline with counted vmcnt waits (saddr addressing, loads into dead fragment registers)
# speedup vs baseline: 1.0221x; 1.0221x over previous
.LBB0_1150:
	v_lshl_or_b32 v6, s71, 8, v202
	v_ashrrev_i32_e32 v7, 31, v6
	v_add_u32_e32 v10, s70, v200
	v_lshl_add_u64 v[8:9], v[6:7], 2, s[14:15]
	v_ashrrev_i32_e32 v11, 31, v10
	global_load_dwordx4 v[16:19], v[8:9], off
	global_load_dwordx4 v[20:23], v[8:9], off offset:64
	global_load_dwordx4 v[24:27], v[8:9], off offset:512
	global_load_dwordx4 v[28:31], v[8:9], off offset:576
	v_lshlrev_b64 v[10:11], 11, v[10:11]
	v_lshl_add_u64 v[6:7], v[10:11], 0, v[6:7]
	v_lshlrev_b32_e32 v14, 2, v6
	global_load_dwordx4 v[212:215], v14, s[6:7]
	global_load_dwordx4 v[216:219], v14, s[6:7] offset:64
	global_load_dwordx4 v[220:223], v14, s[6:7] offset:512
	global_load_dwordx4 v[224:227], v14, s[6:7] offset:576
	v_add_u32_e32 v12, s24, v14
	global_load_dwordx4 v[228:231], v12, s[6:7]
	global_load_dwordx4 v[232:235], v12, s[6:7] offset:64
	global_load_dwordx4 v[236:239], v12, s[6:7] offset:512
	global_load_dwordx4 v[240:243], v12, s[6:7] offset:576
	v_add_u32_e32 v12, s10, v14
	global_load_dwordx4 v[244:247], v12, s[6:7]
	global_load_dwordx4 v[248:251], v12, s[6:7] offset:64
	global_load_dwordx4 v[2:5], v12, s[6:7] offset:512
	global_load_dwordx4 v[8:11], v12, s[6:7] offset:576
	s_andn2_b64 vcc, exec, s[0:1]
	s_mov_b64 s[0:1], -1
	s_nop 15
	s_waitcnt vmcnt(12)
	v_pk_mul_f32 v[16:17], v[16:17], s[22:23] op_sel_hi:[1,0]
	v_pk_mul_f32 v[18:19], v[18:19], s[22:23] op_sel_hi:[1,0]
	v_pk_mul_f32 v[20:21], v[20:21], s[22:23] op_sel_hi:[1,0]
	v_pk_mul_f32 v[22:23], v[22:23], s[22:23] op_sel_hi:[1,0]
	v_pk_mul_f32 v[24:25], v[24:25], s[22:23] op_sel_hi:[1,0]
	v_pk_mul_f32 v[26:27], v[26:27], s[22:23] op_sel_hi:[1,0]
	v_pk_mul_f32 v[28:29], v[28:29], s[22:23] op_sel_hi:[1,0]
	v_pk_mul_f32 v[30:31], v[30:31], s[22:23] op_sel_hi:[1,0]
	s_waitcnt vmcnt(8)
	v_pk_fma_f32 v[214:215], v[160:161], v[18:19], v[214:215]
	v_pk_fma_f32 v[212:213], v[158:159], v[16:17], v[212:213]
	v_pk_fma_f32 v[218:219], v[156:157], v[22:23], v[218:219]
	v_pk_fma_f32 v[216:217], v[154:155], v[20:21], v[216:217]
	v_pk_fma_f32 v[222:223], v[152:153], v[26:27], v[222:223]
	v_pk_fma_f32 v[220:221], v[150:151], v[24:25], v[220:221]
	v_pk_fma_f32 v[226:227], v[140:141], v[30:31], v[226:227]
	v_pk_fma_f32 v[224:225], v[138:139], v[28:29], v[224:225]
	global_store_dwordx4 v14, v[212:215], s[48:49]
	global_store_dwordx4 v14, v[216:219], s[48:49] offset:64
	global_store_dwordx4 v14, v[220:223], s[48:49] offset:512
	global_store_dwordx4 v14, v[224:227], s[48:49] offset:576
	v_add_u32_e32 v12, s26, v14
	global_load_dwordx4 v[212:215], v12, s[6:7]
	global_load_dwordx4 v[216:219], v12, s[6:7] offset:64
	global_load_dwordx4 v[220:223], v12, s[6:7] offset:512
	global_load_dwordx4 v[224:227], v12, s[6:7] offset:576
	s_waitcnt vmcnt(12)
	v_pk_fma_f32 v[230:231], v[148:149], v[18:19], v[230:231]
	v_pk_fma_f32 v[228:229], v[146:147], v[16:17], v[228:229]
	v_pk_fma_f32 v[234:235], v[144:145], v[22:23], v[234:235]
	v_pk_fma_f32 v[232:233], v[142:143], v[20:21], v[232:233]
	v_pk_fma_f32 v[238:239], v[136:137], v[26:27], v[238:239]
	v_pk_fma_f32 v[236:237], v[134:135], v[24:25], v[236:237]
	v_pk_fma_f32 v[242:243], v[124:125], v[30:31], v[242:243]
	v_pk_fma_f32 v[240:241], v[122:123], v[28:29], v[240:241]
	v_add_u32_e32 v13, s24, v14
	global_store_dwordx4 v13, v[228:231], s[48:49]
	global_store_dwordx4 v13, v[232:235], s[48:49] offset:64
	global_store_dwordx4 v13, v[236:239], s[48:49] offset:512
	global_store_dwordx4 v13, v[240:243], s[48:49] offset:576
	v_add_u32_e32 v12, s28, v14
	global_load_dwordx4 v[228:231], v12, s[6:7]
	global_load_dwordx4 v[232:235], v12, s[6:7] offset:64
	global_load_dwordx4 v[236:239], v12, s[6:7] offset:512
	global_load_dwordx4 v[240:243], v12, s[6:7] offset:576
	s_waitcnt vmcnt(16)
	v_pk_fma_f32 v[246:247], v[132:133], v[18:19], v[246:247]
	v_pk_fma_f32 v[244:245], v[130:131], v[16:17], v[244:245]
	v_pk_fma_f32 v[250:251], v[128:129], v[22:23], v[250:251]
	v_pk_fma_f32 v[248:249], v[126:127], v[20:21], v[248:249]
	v_pk_fma_f32 v[4:5], v[120:121], v[26:27], v[4:5]
	v_pk_fma_f32 v[2:3], v[118:119], v[24:25], v[2:3]
	v_pk_fma_f32 v[10:11], v[108:109], v[30:31], v[10:11]
	v_pk_fma_f32 v[8:9], v[106:107], v[28:29], v[8:9]
	v_add_u32_e32 v13, s10, v14
	global_store_dwordx4 v13, v[244:247], s[48:49]
	global_store_dwordx4 v13, v[248:251], s[48:49] offset:64
	global_store_dwordx4 v13, v[2:5], s[48:49] offset:512
	global_store_dwordx4 v13, v[8:11], s[48:49] offset:576
	v_add_u32_e32 v12, s30, v14
	global_load_dwordx4 v[244:247], v12, s[6:7]
	global_load_dwordx4 v[248:251], v12, s[6:7] offset:64
	global_load_dwordx4 v[2:5], v12, s[6:7] offset:512
	global_load_dwordx4 v[8:11], v12, s[6:7] offset:576
	s_waitcnt vmcnt(16)
	v_pk_fma_f32 v[214:215], v[116:117], v[18:19], v[214:215]
	v_pk_fma_f32 v[212:213], v[114:115], v[16:17], v[212:213]
	v_pk_fma_f32 v[218:219], v[112:113], v[22:23], v[218:219]
	v_pk_fma_f32 v[216:217], v[110:111], v[20:21], v[216:217]
	v_pk_fma_f32 v[222:223], v[104:105], v[26:27], v[222:223]
	v_pk_fma_f32 v[220:221], v[102:103], v[24:25], v[220:221]
	v_pk_fma_f32 v[226:227], v[100:101], v[30:31], v[226:227]
	v_pk_fma_f32 v[224:225], v[98:99], v[28:29], v[224:225]
	v_add_u32_e32 v13, s26, v14
	global_store_dwordx4 v13, v[212:215], s[48:49]
	global_store_dwordx4 v13, v[216:219], s[48:49] offset:64
	global_store_dwordx4 v13, v[220:223], s[48:49] offset:512
	global_store_dwordx4 v13, v[224:227], s[48:49] offset:576
	v_add_u32_e32 v12, s34, v14
	global_load_dwordx4 v[212:215], v12, s[6:7]
	global_load_dwordx4 v[216:219], v12, s[6:7] offset:64
	global_load_dwordx4 v[220:223], v12, s[6:7] offset:512
	global_load_dwordx4 v[224:227], v12, s[6:7] offset:576
	s_waitcnt vmcnt(16)
	v_pk_fma_f32 v[230:231], v[96:97], v[18:19], v[230:231]
	v_pk_fma_f32 v[228:229], v[94:95], v[16:17], v[228:229]
	v_pk_fma_f32 v[234:235], v[92:93], v[22:23], v[234:235]
	v_pk_fma_f32 v[232:233], v[90:91], v[20:21], v[232:233]
	v_pk_fma_f32 v[238:239], v[88:89], v[26:27], v[238:239]
	v_pk_fma_f32 v[236:237], v[86:87], v[24:25], v[236:237]
	v_pk_fma_f32 v[242:243], v[76:77], v[30:31], v[242:243]
	v_pk_fma_f32 v[240:241], v[74:75], v[28:29], v[240:241]
	v_add_u32_e32 v13, s28, v14
	global_store_dwordx4 v13, v[228:231], s[48:49]
	global_store_dwordx4 v13, v[232:235], s[48:49] offset:64
	global_store_dwordx4 v13, v[236:239], s[48:49] offset:512
	global_store_dwordx4 v13, v[240:243], s[48:49] offset:576
	v_add_u32_e32 v12, s36, v14
	global_load_dwordx4 v[228:231], v12, s[6:7]
	global_load_dwordx4 v[232:235], v12, s[6:7] offset:64
	global_load_dwordx4 v[236:239], v12, s[6:7] offset:512
	global_load_dwordx4 v[240:243], v12, s[6:7] offset:576
	s_waitcnt vmcnt(16)
	v_pk_fma_f32 v[246:247], v[84:85], v[18:19], v[246:247]
	v_pk_fma_f32 v[244:245], v[82:83], v[16:17], v[244:245]
	v_pk_fma_f32 v[250:251], v[80:81], v[22:23], v[250:251]
	v_pk_fma_f32 v[248:249], v[78:79], v[20:21], v[248:249]
	v_pk_fma_f32 v[4:5], v[72:73], v[26:27], v[4:5]
	v_pk_fma_f32 v[2:3], v[70:71], v[24:25], v[2:3]
	v_pk_fma_f32 v[10:11], v[60:61], v[30:31], v[10:11]
	v_pk_fma_f32 v[8:9], v[58:59], v[28:29], v[8:9]
	v_add_u32_e32 v13, s30, v14
	global_store_dwordx4 v13, v[244:247], s[48:49]
	global_store_dwordx4 v13, v[248:251], s[48:49] offset:64
	global_store_dwordx4 v13, v[2:5], s[48:49] offset:512
	global_store_dwordx4 v13, v[8:11], s[48:49] offset:576
	s_waitcnt vmcnt(12)
	v_pk_fma_f32 v[214:215], v[68:69], v[18:19], v[214:215]
	v_pk_fma_f32 v[212:213], v[66:67], v[16:17], v[212:213]
	v_pk_fma_f32 v[218:219], v[64:65], v[22:23], v[218:219]
	v_pk_fma_f32 v[216:217], v[62:63], v[20:21], v[216:217]
	v_pk_fma_f32 v[222:223], v[56:57], v[26:27], v[222:223]
	v_pk_fma_f32 v[220:221], v[54:55], v[24:25], v[220:221]
	v_pk_fma_f32 v[226:227], v[44:45], v[30:31], v[226:227]
	v_pk_fma_f32 v[224:225], v[42:43], v[28:29], v[224:225]
	v_add_u32_e32 v13, s34, v14
	global_store_dwordx4 v13, v[212:215], s[48:49]
	global_store_dwordx4 v13, v[216:219], s[48:49] offset:64
	global_store_dwordx4 v13, v[220:223], s[48:49] offset:512
	global_store_dwordx4 v13, v[224:227], s[48:49] offset:576
	s_waitcnt vmcnt(8)
	v_pk_fma_f32 v[230:231], v[52:53], v[18:19], v[230:231]
	v_pk_fma_f32 v[228:229], v[50:51], v[16:17], v[228:229]
	v_pk_fma_f32 v[234:235], v[48:49], v[22:23], v[234:235]
	v_pk_fma_f32 v[232:233], v[46:47], v[20:21], v[232:233]
	v_pk_fma_f32 v[238:239], v[40:41], v[26:27], v[238:239]
	v_pk_fma_f32 v[236:237], v[38:39], v[24:25], v[236:237]
	v_pk_fma_f32 v[242:243], v[36:37], v[30:31], v[242:243]
	v_pk_fma_f32 v[240:241], v[34:35], v[28:29], v[240:241]
	v_add_u32_e32 v13, s36, v14
	global_store_dwordx4 v13, v[228:231], s[48:49]
	global_store_dwordx4 v13, v[232:235], s[48:49] offset:64
	global_store_dwordx4 v13, v[236:239], s[48:49] offset:512
	global_store_dwordx4 v13, v[240:243], s[48:49] offset:576
	s_cbranch_vccnz .LBB0_1134
	s_andn2_b64 vcc, exec, s[12:13]
	s_cbranch_vccnz .LBB0_1133
	s_barrier
	s_branch .LBB0_1133
